# v24 + phase-0 XCD-aware item swizzle (bid_eff = bid[1:0] | bid[7:3]<<2 | bid[2]<<7 for the transposer induction variables: 32 consecutive n-blocks of one k-group per XCD so shared 128 B lines hit L2)
# baseline (speedup 1.0000x reference)
.LBB0_7:
	s_load_dwordx16 s[64:79], s[0:1], 0x50
	s_load_dwordx16 s[36:51], s[0:1], 0x90
	s_lshl_b32 s94, s97, 3
	s_cmp_lt_i32 s90, 1
	s_cselect_b64 s[0:1], -1, 0
	s_cmp_gt_i32 s91, 0
	s_waitcnt lgkmcnt(0)
	v_writelane_b32 v239, s36, 7
	s_cselect_b64 s[2:3], -1, 0
	s_lshl_b32 s83, s96, 3
	v_writelane_b32 v239, s37, 8
	v_writelane_b32 v239, s38, 9
	v_writelane_b32 v239, s39, 10
	v_writelane_b32 v239, s40, 11
	v_writelane_b32 v239, s41, 12
	v_writelane_b32 v239, s42, 13
	v_writelane_b32 v239, s43, 14
	v_writelane_b32 v239, s44, 15
	v_writelane_b32 v239, s45, 16
	v_writelane_b32 v239, s46, 17
	v_writelane_b32 v239, s47, 18
	v_writelane_b32 v239, s48, 19
	v_writelane_b32 v239, s49, 20
	v_writelane_b32 v239, s50, 21
	v_writelane_b32 v239, s51, 22
	v_writelane_b32 v239, s83, 23
	v_writelane_b32 v239, s88, 24
	s_and_b64 s[0:1], s[0:1], s[2:3]
	s_andn2_b64 vcc, exec, s[0:1]
	v_writelane_b32 v239, s89, 25
	v_writelane_b32 v239, s90, 26
	v_writelane_b32 v239, s91, 27
	s_cbranch_vccnz .LBB0_175
	v_mov_b32_e32 v1, v0
	s_lshl_b32 s39, s96, 9
	v_readfirstlane_b32 s0, v1
	s_ashr_i32 s0, s0, 6
	s_lshl_b32 s52, s97, 9
	s_add_i32 s62, s0, s83
	s_mov_b32 s98, s96
	s_cmpk_lg_u32 s97, 0x100
	s_cbranch_scc1 .Lxs_done
	s_and_b32 s98, s96, 3
	s_bfe_u32 s62, s96, 0x50003
	s_lshl_b32 s62, s62, 2
	s_or_b32 s98, s98, s62
	s_bfe_u32 s62, s96, 0x10002
	s_lshl_b32 s62, s62, 7
	s_or_b32 s98, s98, s62
.Lxs_done:
	s_lshl_b32 s62, s98, 3
	s_add_i32 s62, s0, s62
	s_mov_b32 s2, s94
	s_cmpk_lt_i32 s62, 0x7600
	v_writelane_b32 v239, s2, 28
	s_nop 1
	v_writelane_b32 v239, s3, 29
	s_cbranch_scc0 .LBB0_102
	s_mul_i32 s1, s0, 0x4100
	v_writelane_b32 v239, s33, 30
	s_add_i32 s41, s1, 0
	v_writelane_b32 v239, s1, 31
	s_add_u32 s1, s88, 0xd900000
	v_writelane_b32 v239, s1, 33
	s_addc_u32 s1, s89, 0
	v_writelane_b32 v239, s1, 35
	s_add_u32 s1, s88, 0xb900000
	v_writelane_b32 v239, s1, 37
	s_addc_u32 s1, s89, 0
	v_writelane_b32 v239, s1, 39
	s_add_u32 s1, s88, 0x7900000
	v_writelane_b32 v239, s1, 40
	s_addc_u32 s1, s89, 0
	s_add_u32 s95, s88, 0x100000
	v_writelane_b32 v239, s1, 42
	s_addc_u32 s44, s89, 0
	s_lshl_b32 s1, s0, 6
	s_lshl_b32 s3, s98, 9
	s_add_i32 s3, s3, s1
	s_lshl_b32 s1, s98, 4
	s_lshl_b32 s0, s0, 1
	s_add_i32 s9, s1, s0
	s_lshl_b32 s0, s62, 2
	v_and_b32_e32 v136, 63, v1
	s_mov_b32 s92, 0
	v_writelane_b32 v239, s96, 44
	s_lshl_b32 s96, s97, 4
	s_add_i32 s36, s0, 0xffff4400
	s_lshl_b32 s2, s97, 5
	s_mov_b64 s[0:1], 0
	s_mov_b32 s37, s3
	s_mov_b32 s33, s62
	s_mov_b64 s[4:5], 0
	s_mov_b32 s91, 0
	s_mov_b32 s6, 0
	s_mov_b32 s8, 0
	s_mov_b32 s60, 0
	s_mov_b32 s61, 0
	s_mov_b32 s40, s95
